# kernel-start silu(c) staging loop: 16 serial load/wait round trips per thread replaced by 16 loads in flight and one wait (both role copies); on top of nt weight loads
# speedup vs baseline: 1.0128x; 1.0128x over previous
.LBB0_147:
	global_load_dword v12, v[8:9], off
	v_lshl_add_u64 v[8:9], v[8:9], 0, s[2:3]
	global_load_dword v13, v[8:9], off
	v_lshl_add_u64 v[8:9], v[8:9], 0, s[2:3]
	global_load_dword v14, v[8:9], off
	v_lshl_add_u64 v[8:9], v[8:9], 0, s[2:3]
	global_load_dword v15, v[8:9], off
	v_lshl_add_u64 v[8:9], v[8:9], 0, s[2:3]
	global_load_dword v16, v[8:9], off
	v_lshl_add_u64 v[8:9], v[8:9], 0, s[2:3]
	global_load_dword v17, v[8:9], off
	v_lshl_add_u64 v[8:9], v[8:9], 0, s[2:3]
	global_load_dword v18, v[8:9], off
	v_lshl_add_u64 v[8:9], v[8:9], 0, s[2:3]
	global_load_dword v19, v[8:9], off
	v_lshl_add_u64 v[8:9], v[8:9], 0, s[2:3]
	global_load_dword v20, v[8:9], off
	v_lshl_add_u64 v[8:9], v[8:9], 0, s[2:3]
	global_load_dword v21, v[8:9], off
	v_lshl_add_u64 v[8:9], v[8:9], 0, s[2:3]
	global_load_dword v22, v[8:9], off
	v_lshl_add_u64 v[8:9], v[8:9], 0, s[2:3]
	global_load_dword v23, v[8:9], off
	v_lshl_add_u64 v[8:9], v[8:9], 0, s[2:3]
	global_load_dword v24, v[8:9], off
	v_lshl_add_u64 v[8:9], v[8:9], 0, s[2:3]
	global_load_dword v25, v[8:9], off
	v_lshl_add_u64 v[8:9], v[8:9], 0, s[2:3]
	global_load_dword v26, v[8:9], off
	v_lshl_add_u64 v[8:9], v[8:9], 0, s[2:3]
	global_load_dword v27, v[8:9], off
	s_waitcnt vmcnt(0)
	v_mul_f32_e32 v28, 0xbfb8aa3b, v12
	v_mul_f32_e32 v29, 0xbfb8aa3b, v13
	v_mul_f32_e32 v30, 0xbfb8aa3b, v14
	v_mul_f32_e32 v31, 0xbfb8aa3b, v15
	v_exp_f32_e32 v28, v28
	v_exp_f32_e32 v29, v29
	v_exp_f32_e32 v30, v30
	v_exp_f32_e32 v31, v31
	v_add_f32_e32 v28, 1.0, v28
	v_add_f32_e32 v29, 1.0, v29
	v_add_f32_e32 v30, 1.0, v30
	v_add_f32_e32 v31, 1.0, v31
	v_rcp_f32_e32 v28, v28
	v_rcp_f32_e32 v29, v29
	v_rcp_f32_e32 v30, v30
	v_rcp_f32_e32 v31, v31
	v_mul_f32_e32 v12, v12, v28
	v_mul_f32_e32 v13, v13, v29
	v_mul_f32_e32 v14, v14, v30
	v_mul_f32_e32 v15, v15, v31
	ds_write_b32 v1, v12
	ds_write_b32 v1, v13 offset:2048
	ds_write_b32 v1, v14 offset:4096
	ds_write_b32 v1, v15 offset:6144
	v_mul_f32_e32 v28, 0xbfb8aa3b, v16
	v_mul_f32_e32 v29, 0xbfb8aa3b, v17
	v_mul_f32_e32 v30, 0xbfb8aa3b, v18
	v_mul_f32_e32 v31, 0xbfb8aa3b, v19
	v_exp_f32_e32 v28, v28
	v_exp_f32_e32 v29, v29
	v_exp_f32_e32 v30, v30
	v_exp_f32_e32 v31, v31
	v_add_f32_e32 v28, 1.0, v28
	v_add_f32_e32 v29, 1.0, v29
	v_add_f32_e32 v30, 1.0, v30
	v_add_f32_e32 v31, 1.0, v31
	v_rcp_f32_e32 v28, v28
	v_rcp_f32_e32 v29, v29
	v_rcp_f32_e32 v30, v30
	v_rcp_f32_e32 v31, v31
	v_mul_f32_e32 v16, v16, v28
	v_mul_f32_e32 v17, v17, v29
	v_mul_f32_e32 v18, v18, v30
	v_mul_f32_e32 v19, v19, v31
	ds_write_b32 v1, v16 offset:8192
	ds_write_b32 v1, v17 offset:10240
	ds_write_b32 v1, v18 offset:12288
	ds_write_b32 v1, v19 offset:14336
	v_mul_f32_e32 v28, 0xbfb8aa3b, v20
	v_mul_f32_e32 v29, 0xbfb8aa3b, v21
	v_mul_f32_e32 v30, 0xbfb8aa3b, v22
	v_mul_f32_e32 v31, 0xbfb8aa3b, v23
	v_exp_f32_e32 v28, v28
	v_exp_f32_e32 v29, v29
	v_exp_f32_e32 v30, v30
	v_exp_f32_e32 v31, v31
	v_add_f32_e32 v28, 1.0, v28
	v_add_f32_e32 v29, 1.0, v29
	v_add_f32_e32 v30, 1.0, v30
	v_add_f32_e32 v31, 1.0, v31
	v_rcp_f32_e32 v28, v28
	v_rcp_f32_e32 v29, v29
	v_rcp_f32_e32 v30, v30
	v_rcp_f32_e32 v31, v31
	v_mul_f32_e32 v20, v20, v28
	v_mul_f32_e32 v21, v21, v29
	v_mul_f32_e32 v22, v22, v30
	v_mul_f32_e32 v23, v23, v31
	ds_write_b32 v1, v20 offset:16384
	ds_write_b32 v1, v21 offset:18432
	ds_write_b32 v1, v22 offset:20480
	ds_write_b32 v1, v23 offset:22528
	v_mul_f32_e32 v28, 0xbfb8aa3b, v24
	v_mul_f32_e32 v29, 0xbfb8aa3b, v25
	v_mul_f32_e32 v30, 0xbfb8aa3b, v26
	v_mul_f32_e32 v31, 0xbfb8aa3b, v27
	v_exp_f32_e32 v28, v28
	v_exp_f32_e32 v29, v29
	v_exp_f32_e32 v30, v30
	v_exp_f32_e32 v31, v31
	v_add_f32_e32 v28, 1.0, v28
	v_add_f32_e32 v29, 1.0, v29
	v_add_f32_e32 v30, 1.0, v30
	v_add_f32_e32 v31, 1.0, v31
	v_rcp_f32_e32 v28, v28
	v_rcp_f32_e32 v29, v29
	v_rcp_f32_e32 v30, v30
	v_rcp_f32_e32 v31, v31
	v_mul_f32_e32 v24, v24, v28
	v_mul_f32_e32 v25, v25, v29
	v_mul_f32_e32 v26, v26, v30
	v_mul_f32_e32 v27, v27, v31
	ds_write_b32 v1, v24 offset:24576
	ds_write_b32 v1, v25 offset:26624
	ds_write_b32 v1, v26 offset:28672
	ds_write_b32 v1, v27 offset:30720
	s_or_b64 exec, exec, s[0:1]
	s_cmpk_lt_u32 s96, 0x280
	s_waitcnt lgkmcnt(0)
	s_barrier
	s_cbranch_scc0 .LBB0_157
	s_add_i32 s0, s96, 0x80
	s_lshl_b32 s1, s0, 4
	s_and_b32 s1, s1, 0x7fe0
	v_and_b32_e32 v159, 28, v6
	s_lshl_b32 s0, s0, 10
	v_lshrrev_b32_e32 v1, 3, v0
	v_or_b32_e32 v7, s1, v159
	s_and_b32 s0, s0, 0x400
	v_or_b32_e32 v10, s0, v1
	v_lshlrev_b32_e32 v134, 2, v7
	v_mov_b32_e32 v135, 0
	v_lshl_add_u64 v[8:9], s[16:17], 0, v[134:135]
	v_mul_u32_u24_e32 v134, 0xc000, v10
	v_lshl_add_u64 v[8:9], v[8:9], 0, v[134:135]
	s_mov_b32 s1, 0x600000
	v_add_co_u32_e32 v10, vcc, s1, v8
	s_mov_b32 s1, 0x900000
	s_nop 0
	v_addc_co_u32_e32 v11, vcc, 0, v9, vcc
	v_add_co_u32_e32 v12, vcc, s1, v8
	s_mov_b32 s1, 0xc00000
	s_nop 0
	v_addc_co_u32_e32 v13, vcc, 0, v9, vcc
	global_load_dwordx4 v[114:117], v[10:11], off nt
	global_load_dwordx4 v[118:121], v[12:13], off nt
	v_add_co_u32_e32 v10, vcc, s1, v8
	s_mov_b32 s1, 0xf00000
	s_nop 0
	v_addc_co_u32_e32 v11, vcc, 0, v9, vcc
	v_add_co_u32_e32 v12, vcc, s1, v8
	s_mov_b32 s1, 0x1200000
	s_nop 0
	v_addc_co_u32_e32 v13, vcc, 0, v9, vcc
	v_add_co_u32_e32 v14, vcc, s1, v8
	s_mov_b32 s1, 0x1500000
	s_nop 0
	v_addc_co_u32_e32 v15, vcc, 0, v9, vcc
	v_add_co_u32_e32 v16, vcc, s1, v8
	s_mov_b32 s1, 0x1800000
	s_nop 0
	v_addc_co_u32_e32 v17, vcc, 0, v9, vcc
	v_add_co_u32_e32 v18, vcc, s1, v8
	s_mov_b32 s1, 0x1b00000
	s_nop 0
	v_addc_co_u32_e32 v19, vcc, 0, v9, vcc
	v_add_co_u32_e32 v20, vcc, s1, v8
	s_mov_b32 s1, 0x1e00000
	s_nop 0
	v_addc_co_u32_e32 v21, vcc, 0, v9, vcc
	v_add_co_u32_e32 v22, vcc, s1, v8
	s_mov_b32 s1, 0x2100000
	s_nop 0
	v_addc_co_u32_e32 v23, vcc, 0, v9, vcc
	v_add_co_u32_e32 v24, vcc, s1, v8
	s_mov_b32 s1, 0x2400000
	s_nop 0
	v_addc_co_u32_e32 v25, vcc, 0, v9, vcc
	v_add_co_u32_e32 v26, vcc, s1, v8
	s_mov_b32 s1, 0x2700000
	s_nop 0
	v_addc_co_u32_e32 v27, vcc, 0, v9, vcc
	v_add_co_u32_e32 v28, vcc, s1, v8
	s_mov_b32 s1, 0x2a00000
	s_nop 0
	v_addc_co_u32_e32 v29, vcc, 0, v9, vcc
	v_add_co_u32_e32 v30, vcc, s1, v8
	s_mov_b32 s1, 0x2d00000
	s_nop 0
	v_addc_co_u32_e32 v31, vcc, 0, v9, vcc
	v_add_co_u32_e32 v32, vcc, s1, v8
	s_mov_b32 s0, 0x300000
	s_nop 0
	v_addc_co_u32_e32 v33, vcc, 0, v9, vcc
	global_load_dwordx4 v[70:73], v[30:31], off nt
	global_load_dwordx4 v[74:77], v[32:33], off nt
	global_load_dwordx4 v[82:85], v[26:27], off nt
	global_load_dwordx4 v[78:81], v[28:29], off nt
	global_load_dwordx4 v[90:93], v[22:23], off nt
	global_load_dwordx4 v[86:89], v[24:25], off nt
	global_load_dwordx4 v[98:101], v[18:19], off nt
	global_load_dwordx4 v[94:97], v[20:21], off nt
	global_load_dwordx4 v[106:109], v[14:15], off nt
	global_load_dwordx4 v[102:105], v[16:17], off nt
	global_load_dwordx4 v[122:125], v[10:11], off nt
	global_load_dwordx4 v[110:113], v[12:13], off nt
	v_add_co_u32_e32 v10, vcc, s0, v8
	s_and_b32 s4, s96, 1
	s_nop 0
	v_addc_co_u32_e32 v11, vcc, 0, v9, vcc
	global_load_dwordx4 v[126:129], v[10:11], off nt
	global_load_dwordx4 v[130:133], v[8:9], off nt
	v_lshrrev_b32_e32 v9, 5, v0
	s_lshl_b32 s1, s4, 12
	v_and_b32_e32 v10, 0x70, v6
	v_mul_u32_u24_e32 v6, 0x3000, v9
	s_add_i32 s1, s1, 0
	v_lshlrev_b32_e32 v134, 2, v6
	v_and_b32_e32 v11, 3, v0
	v_lshl_add_u64 v[6:7], s[70:71], 0, v[134:135]
	s_mov_b64 s[2:3], 0x8000
	s_cmp_eq_u32 s4, 0
	v_lshlrev_b32_e32 v8, 6, v0
	v_lshl_add_u64 v[136:137], v[6:7], 0, s[2:3]
	s_cselect_b64 s[2:3], -1, 0
	v_lshl_add_u32 v6, v9, 4, 0
	v_lshlrev_b32_e32 v7, 2, v11
	v_lshlrev_b32_e32 v9, 2, v10
	s_lshl_b32 s4, s96, 10
	s_movk_i32 s0, 0x80
	v_add3_u32 v207, v6, v7, v9
	s_add_i32 s8, s4, 0x20000
	s_lshl_b32 s4, s96, 4
	v_add_u32_e32 v208, 0, v8
	s_waitcnt vmcnt(14)
	v_mov_b64_e32 v[18:19], v[118:119]
	v_mov_b64_e32 v[14:15], v[114:115]
	v_lshl_add_u32 v171, v1, 2, s1
	v_cmp_gt_u32_e64 s[0:1], s0, v0
	v_and_b32_e32 v206, 31, v0
	s_add_i32 s9, s4, 0x800
	s_mov_b32 s10, s96
	v_mov_b64_e32 v[20:21], v[120:121]
	v_mov_b64_e32 v[16:17], v[116:117]
	s_waitcnt vmcnt(13)
	v_mov_b64_e32 v[62:63], v[70:71]
	s_waitcnt vmcnt(12)
	v_mov_b64_e32 v[66:67], v[74:75]
	s_waitcnt vmcnt(11)
	v_mov_b64_e32 v[54:55], v[82:83]
	s_waitcnt vmcnt(10)
	v_mov_b64_e32 v[58:59], v[78:79]
	s_waitcnt vmcnt(9)
	v_mov_b64_e32 v[46:47], v[90:91]
	s_waitcnt vmcnt(8)
	v_mov_b64_e32 v[50:51], v[86:87]
	s_waitcnt vmcnt(7)
	v_mov_b64_e32 v[38:39], v[98:99]
	s_waitcnt vmcnt(6)
	v_mov_b64_e32 v[42:43], v[94:95]
	s_waitcnt vmcnt(5)
	v_mov_b64_e32 v[30:31], v[106:107]
	s_waitcnt vmcnt(4)
	v_mov_b64_e32 v[34:35], v[102:103]
	s_waitcnt vmcnt(3)
	v_mov_b64_e32 v[22:23], v[122:123]
	s_waitcnt vmcnt(2)
	v_mov_b64_e32 v[26:27], v[110:111]
	v_mov_b64_e32 v[68:69], v[76:77]
	v_mov_b64_e32 v[64:65], v[72:73]
	v_mov_b64_e32 v[60:61], v[80:81]
	v_mov_b64_e32 v[56:57], v[84:85]
	s_waitcnt vmcnt(1)
	v_mov_b64_e32 v[10:11], v[126:127]
	s_waitcnt vmcnt(0)
	v_mov_b64_e32 v[6:7], v[130:131]
	v_mov_b64_e32 v[52:53], v[88:89]
	v_mov_b64_e32 v[48:49], v[92:93]
	v_mov_b64_e32 v[44:45], v[96:97]
	v_mov_b64_e32 v[40:41], v[100:101]
	v_mov_b64_e32 v[36:37], v[104:105]
	v_mov_b64_e32 v[32:33], v[108:109]
	v_mov_b64_e32 v[28:29], v[112:113]
	v_mov_b64_e32 v[24:25], v[124:125]
	v_mov_b64_e32 v[12:13], v[128:129]
	v_mov_b64_e32 v[8:9], v[132:133]
	s_branch .LBB0_152

.LBB0_223:
	global_load_dword v12, v[6:7], off
	v_lshl_add_u64 v[6:7], v[6:7], 0, s[2:3]
	global_load_dword v13, v[6:7], off
	v_lshl_add_u64 v[6:7], v[6:7], 0, s[2:3]
	global_load_dword v14, v[6:7], off
	v_lshl_add_u64 v[6:7], v[6:7], 0, s[2:3]
	global_load_dword v15, v[6:7], off
	v_lshl_add_u64 v[6:7], v[6:7], 0, s[2:3]
	global_load_dword v16, v[6:7], off
	v_lshl_add_u64 v[6:7], v[6:7], 0, s[2:3]
	global_load_dword v17, v[6:7], off
	v_lshl_add_u64 v[6:7], v[6:7], 0, s[2:3]
	global_load_dword v18, v[6:7], off
	v_lshl_add_u64 v[6:7], v[6:7], 0, s[2:3]
	global_load_dword v19, v[6:7], off
	v_lshl_add_u64 v[6:7], v[6:7], 0, s[2:3]
	global_load_dword v20, v[6:7], off
	v_lshl_add_u64 v[6:7], v[6:7], 0, s[2:3]
	global_load_dword v21, v[6:7], off
	v_lshl_add_u64 v[6:7], v[6:7], 0, s[2:3]
	global_load_dword v22, v[6:7], off
	v_lshl_add_u64 v[6:7], v[6:7], 0, s[2:3]
	global_load_dword v23, v[6:7], off
	v_lshl_add_u64 v[6:7], v[6:7], 0, s[2:3]
	global_load_dword v24, v[6:7], off
	v_lshl_add_u64 v[6:7], v[6:7], 0, s[2:3]
	global_load_dword v25, v[6:7], off
	v_lshl_add_u64 v[6:7], v[6:7], 0, s[2:3]
	global_load_dword v26, v[6:7], off
	v_lshl_add_u64 v[6:7], v[6:7], 0, s[2:3]
	global_load_dword v27, v[6:7], off
	s_waitcnt vmcnt(0)
	v_mul_f32_e32 v28, 0xbfb8aa3b, v12
	v_mul_f32_e32 v29, 0xbfb8aa3b, v13
	v_mul_f32_e32 v30, 0xbfb8aa3b, v14
	v_mul_f32_e32 v31, 0xbfb8aa3b, v15
	v_exp_f32_e32 v28, v28
	v_exp_f32_e32 v29, v29
	v_exp_f32_e32 v30, v30
	v_exp_f32_e32 v31, v31
	v_add_f32_e32 v28, 1.0, v28
	v_add_f32_e32 v29, 1.0, v29
	v_add_f32_e32 v30, 1.0, v30
	v_add_f32_e32 v31, 1.0, v31
	v_rcp_f32_e32 v28, v28
	v_rcp_f32_e32 v29, v29
	v_rcp_f32_e32 v30, v30
	v_rcp_f32_e32 v31, v31
	v_mul_f32_e32 v12, v12, v28
	v_mul_f32_e32 v13, v13, v29
	v_mul_f32_e32 v14, v14, v30
	v_mul_f32_e32 v15, v15, v31
	ds_write_b32 v1, v12
	ds_write_b32 v1, v13 offset:2048
	ds_write_b32 v1, v14 offset:4096
	ds_write_b32 v1, v15 offset:6144
	v_mul_f32_e32 v28, 0xbfb8aa3b, v16
	v_mul_f32_e32 v29, 0xbfb8aa3b, v17
	v_mul_f32_e32 v30, 0xbfb8aa3b, v18
	v_mul_f32_e32 v31, 0xbfb8aa3b, v19
	v_exp_f32_e32 v28, v28
	v_exp_f32_e32 v29, v29
	v_exp_f32_e32 v30, v30
	v_exp_f32_e32 v31, v31
	v_add_f32_e32 v28, 1.0, v28
	v_add_f32_e32 v29, 1.0, v29
	v_add_f32_e32 v30, 1.0, v30
	v_add_f32_e32 v31, 1.0, v31
	v_rcp_f32_e32 v28, v28
	v_rcp_f32_e32 v29, v29
	v_rcp_f32_e32 v30, v30
	v_rcp_f32_e32 v31, v31
	v_mul_f32_e32 v16, v16, v28
	v_mul_f32_e32 v17, v17, v29
	v_mul_f32_e32 v18, v18, v30
	v_mul_f32_e32 v19, v19, v31
	ds_write_b32 v1, v16 offset:8192
	ds_write_b32 v1, v17 offset:10240
	ds_write_b32 v1, v18 offset:12288
	ds_write_b32 v1, v19 offset:14336
	v_mul_f32_e32 v28, 0xbfb8aa3b, v20
	v_mul_f32_e32 v29, 0xbfb8aa3b, v21
	v_mul_f32_e32 v30, 0xbfb8aa3b, v22
	v_mul_f32_e32 v31, 0xbfb8aa3b, v23
	v_exp_f32_e32 v28, v28
	v_exp_f32_e32 v29, v29
	v_exp_f32_e32 v30, v30
	v_exp_f32_e32 v31, v31
	v_add_f32_e32 v28, 1.0, v28
	v_add_f32_e32 v29, 1.0, v29
	v_add_f32_e32 v30, 1.0, v30
	v_add_f32_e32 v31, 1.0, v31
	v_rcp_f32_e32 v28, v28
	v_rcp_f32_e32 v29, v29
	v_rcp_f32_e32 v30, v30
	v_rcp_f32_e32 v31, v31
	v_mul_f32_e32 v20, v20, v28
	v_mul_f32_e32 v21, v21, v29
	v_mul_f32_e32 v22, v22, v30
	v_mul_f32_e32 v23, v23, v31
	ds_write_b32 v1, v20 offset:16384
	ds_write_b32 v1, v21 offset:18432
	ds_write_b32 v1, v22 offset:20480
	ds_write_b32 v1, v23 offset:22528
	v_mul_f32_e32 v28, 0xbfb8aa3b, v24
	v_mul_f32_e32 v29, 0xbfb8aa3b, v25
	v_mul_f32_e32 v30, 0xbfb8aa3b, v26
	v_mul_f32_e32 v31, 0xbfb8aa3b, v27
	v_exp_f32_e32 v28, v28
	v_exp_f32_e32 v29, v29
	v_exp_f32_e32 v30, v30
	v_exp_f32_e32 v31, v31
	v_add_f32_e32 v28, 1.0, v28
	v_add_f32_e32 v29, 1.0, v29
	v_add_f32_e32 v30, 1.0, v30
	v_add_f32_e32 v31, 1.0, v31
	v_rcp_f32_e32 v28, v28
	v_rcp_f32_e32 v29, v29
	v_rcp_f32_e32 v30, v30
	v_rcp_f32_e32 v31, v31
	v_mul_f32_e32 v24, v24, v28
	v_mul_f32_e32 v25, v25, v29
	v_mul_f32_e32 v26, v26, v30
	v_mul_f32_e32 v27, v27, v31
	ds_write_b32 v1, v24 offset:24576
	ds_write_b32 v1, v25 offset:26624
	ds_write_b32 v1, v26 offset:28672
	ds_write_b32 v1, v27 offset:30720
	s_or_b64 exec, exec, s[0:1]
	s_lshl_b32 s8, s96, 4
	s_and_b32 s0, s8, 0xffffffe0
	v_and_b32_e32 v159, 28, v134
	s_lshl_b32 s9, s96, 10
	v_lshrrev_b32_e32 v135, 3, v0
	v_or_b32_e32 v6, s0, v159
	s_and_b32 s0, s9, 0x400
	v_or_b32_e32 v1, s0, v135
	v_ashrrev_i32_e32 v7, 31, v6
	v_lshl_add_u64 v[6:7], v[6:7], 2, s[16:17]
	v_mul_u32_u24_e32 v136, 0xc000, v1
	v_mov_b32_e32 v137, 0
	v_lshl_add_u64 v[6:7], v[6:7], 0, v[136:137]
	s_mov_b32 s0, 0x300000
	v_add_co_u32_e32 v8, vcc, s0, v6
	s_mov_b32 s0, 0x600000
	s_nop 0
	v_addc_co_u32_e32 v9, vcc, 0, v7, vcc
	v_add_co_u32_e32 v10, vcc, s0, v6
	s_mov_b32 s0, 0x900000
	s_nop 0
	v_addc_co_u32_e32 v11, vcc, 0, v7, vcc
	v_add_co_u32_e32 v12, vcc, s0, v6
	s_mov_b32 s0, 0xc00000
	s_nop 0
	v_addc_co_u32_e32 v13, vcc, 0, v7, vcc
	v_add_co_u32_e32 v14, vcc, s0, v6
	s_mov_b32 s0, 0xf00000
	s_nop 0
	v_addc_co_u32_e32 v15, vcc, 0, v7, vcc
	v_add_co_u32_e32 v16, vcc, s0, v6
	s_mov_b32 s0, 0x1200000
	s_nop 0
	v_addc_co_u32_e32 v17, vcc, 0, v7, vcc
	v_add_co_u32_e32 v18, vcc, s0, v6
	s_mov_b32 s0, 0x1500000
	s_nop 0
	v_addc_co_u32_e32 v19, vcc, 0, v7, vcc
	v_add_co_u32_e32 v20, vcc, s0, v6
	s_mov_b32 s0, 0x1800000
	s_nop 0
	v_addc_co_u32_e32 v21, vcc, 0, v7, vcc
	v_add_co_u32_e32 v22, vcc, s0, v6
	s_mov_b32 s1, 0x1e00000
	s_nop 0
	v_addc_co_u32_e32 v23, vcc, 0, v7, vcc
	v_add_co_u32_e32 v24, vcc, s1, v6
	s_mov_b32 s1, 0x2100000
	s_nop 0
	v_addc_co_u32_e32 v25, vcc, 0, v7, vcc
	v_add_co_u32_e32 v26, vcc, s1, v6
	s_mov_b32 s1, 0x2400000
	s_nop 0
	v_addc_co_u32_e32 v27, vcc, 0, v7, vcc
	s_waitcnt lgkmcnt(0)
	s_barrier
	global_load_dwordx4 v[70:73], v[24:25], off nt
	global_load_dwordx4 v[74:77], v[26:27], off nt
	v_add_co_u32_e32 v24, vcc, s1, v6
	s_mov_b32 s1, 0x2700000
	s_nop 0
	v_addc_co_u32_e32 v25, vcc, 0, v7, vcc
	v_add_co_u32_e32 v26, vcc, s1, v6
	s_mov_b32 s1, 0x2a00000
	s_nop 0
	v_addc_co_u32_e32 v27, vcc, 0, v7, vcc
	v_add_co_u32_e32 v28, vcc, s1, v6
	s_mov_b32 s1, 0x2d00000
	s_nop 0
	v_addc_co_u32_e32 v29, vcc, 0, v7, vcc
	v_add_co_u32_e32 v30, vcc, s1, v6
	s_mov_b32 s0, 0x1b00000
	s_nop 0
	v_addc_co_u32_e32 v31, vcc, 0, v7, vcc
	global_load_dwordx4 v[78:81], v[28:29], off nt
	global_load_dwordx4 v[82:85], v[30:31], off nt
	global_load_dwordx4 v[90:93], v[24:25], off nt
	global_load_dwordx4 v[86:89], v[26:27], off nt
	v_add_co_u32_e32 v24, vcc, s0, v6
	s_and_b32 s15, s96, 1
	s_nop 0
	v_addc_co_u32_e32 v25, vcc, 0, v7, vcc
	global_load_dwordx4 v[94:97], v[24:25], off nt
	global_load_dwordx4 v[98:101], v[22:23], off nt
	global_load_dwordx4 v[102:105], v[20:21], off nt
	global_load_dwordx4 v[106:109], v[18:19], off nt
	global_load_dwordx4 v[110:113], v[16:17], off nt
	global_load_dwordx4 v[114:117], v[14:15], off nt
	global_load_dwordx4 v[118:121], v[12:13], off nt
	global_load_dwordx4 v[122:125], v[10:11], off nt
	global_load_dwordx4 v[126:129], v[8:9], off nt
	global_load_dwordx4 v[130:133], v[6:7], off nt
	v_lshrrev_b32_e32 v9, 5, v0
	v_mul_u32_u24_e32 v6, 0x3000, v9
	v_lshlrev_b32_e32 v136, 2, v6
	s_lshl_b32 s14, s15, 12
	v_and_b32_e32 v10, 0x70, v134
	v_and_b32_e32 v11, 3, v0
	v_lshl_add_u64 v[6:7], s[70:71], 0, v[136:137]
	s_mov_b64 s[2:3], 0x8000
	v_lshlrev_b32_e32 v8, 6, v0
	s_add_i32 s0, s14, 0
	v_lshl_add_u64 v[138:139], v[6:7], 0, s[2:3]
	v_lshl_add_u32 v6, v9, 4, 0
	v_lshlrev_b32_e32 v7, 2, v11
	v_lshlrev_b32_e32 v9, 2, v10
	v_lshl_add_u32 v171, v135, 2, s0
	s_movk_i32 s0, 0x80
	s_cmp_eq_u32 s15, 0
	v_add3_u32 v208, v6, v7, v9
	v_add_u32_e32 v209, 0, v8
	v_cmp_gt_u32_e64 s[0:1], s0, v0
	v_and_b32_e32 v1, 31, v0
	s_cselect_b64 s[4:5], -1, 0
	s_mov_b32 s10, s96
	s_waitcnt vmcnt(15)
	v_mov_b64_e32 v[46:47], v[70:71]
	s_waitcnt vmcnt(14)
	v_mov_b64_e32 v[50:51], v[74:75]
	v_mov_b64_e32 v[52:53], v[76:77]
	v_mov_b64_e32 v[48:49], v[72:73]
	s_waitcnt vmcnt(13)
	v_mov_b64_e32 v[62:63], v[78:79]
	s_waitcnt vmcnt(12)
	v_mov_b64_e32 v[66:67], v[82:83]
	s_waitcnt vmcnt(11)
	v_mov_b64_e32 v[54:55], v[90:91]
	s_waitcnt vmcnt(10)
	v_mov_b64_e32 v[58:59], v[86:87]
	s_waitcnt vmcnt(9)
	v_mov_b64_e32 v[42:43], v[94:95]
	s_waitcnt vmcnt(8)
	v_mov_b64_e32 v[38:39], v[98:99]
	s_waitcnt vmcnt(7)
	v_mov_b64_e32 v[34:35], v[102:103]
	s_waitcnt vmcnt(6)
	v_mov_b64_e32 v[30:31], v[106:107]
	s_waitcnt vmcnt(5)
	v_mov_b64_e32 v[26:27], v[110:111]
	s_waitcnt vmcnt(4)
	v_mov_b64_e32 v[22:23], v[114:115]
	s_waitcnt vmcnt(3)
	v_mov_b64_e32 v[18:19], v[118:119]
	s_waitcnt vmcnt(2)
	v_mov_b64_e32 v[14:15], v[122:123]
	s_waitcnt vmcnt(1)
	v_mov_b64_e32 v[10:11], v[126:127]
	s_waitcnt vmcnt(0)
	v_mov_b64_e32 v[6:7], v[130:131]
	v_mov_b64_e32 v[68:69], v[84:85]
	v_mov_b64_e32 v[64:65], v[80:81]
	v_mov_b64_e32 v[60:61], v[88:89]
	v_mov_b64_e32 v[56:57], v[92:93]
	v_mov_b64_e32 v[44:45], v[96:97]
	v_mov_b64_e32 v[40:41], v[100:101]
	v_mov_b64_e32 v[36:37], v[104:105]
	v_mov_b64_e32 v[32:33], v[108:109]
	v_mov_b64_e32 v[28:29], v[112:113]
	v_mov_b64_e32 v[24:25], v[116:117]
	v_mov_b64_e32 v[20:21], v[120:121]
	v_mov_b64_e32 v[16:17], v[124:125]
	v_mov_b64_e32 v[12:13], v[128:129]
	v_mov_b64_e32 v[8:9], v[132:133]
	s_branch .LBB0_227
